# row load + causal mask stage: rows loaded straight into rv[], only the boundary 1024-key section's 8 registers masked (scalar branch tree), other sections are guarded by their consumers (on top of v48
# speedup vs baseline: 1.0004x; 1.0004x over previous
.LBB0_720:
	s_or_b64 exec, exec, s[0:1]
	v_readfirstlane_b32 s8, v2
	s_cmp_gt_u32 s8, 31
	s_mov_b64 s[0:1], -1
	s_cbranch_scc1 .LBB0_715
	s_sub_i32 s0, 31, s8
	s_or_b32 s97, s0, s6
	s_lshl_b32 s1, s0, 14
	v_readlane_b32 s8, v254, 51
	s_add_u32 s8, s8, s1
	v_readlane_b32 s1, v254, 52
	v_mov_b32_e32 v10, v200
	s_addc_u32 s9, s1, 0
	s_mov_b32 s1, 0
	v_ashrrev_i32_e32 v11, 31, v10
	s_waitcnt lgkmcnt(0)
	v_lshl_add_u64 v[2:3], v[10:11], 2, s[8:9]
	s_mov_b64 s[10:11], 0x1000
	v_lshl_add_u64 v[4:5], v[2:3], 0, s[10:11]
	s_mov_b64 s[10:11], 0x2000
	v_lshl_add_u64 v[6:7], v[2:3], 0, s[10:11]
	s_mov_b64 s[10:11], 0x3000
	v_lshl_add_u64 v[8:9], v[2:3], 0, s[10:11]
	global_load_dword v77, v[2:3], off
	global_load_dword v76, v[2:3], off offset:256
	global_load_dword v75, v[2:3], off offset:512
	global_load_dword v74, v[2:3], off offset:768
	global_load_dword v73, v[2:3], off offset:1024
	global_load_dword v72, v[2:3], off offset:1280
	global_load_dword v71, v[2:3], off offset:1536
	global_load_dword v70, v[2:3], off offset:1792
	global_load_dword v69, v[2:3], off offset:2048
	global_load_dword v68, v[2:3], off offset:2304
	global_load_dword v67, v[2:3], off offset:2560
	global_load_dword v66, v[2:3], off offset:2816
	global_load_dword v65, v[2:3], off offset:3072
	global_load_dword v64, v[2:3], off offset:3328
	global_load_dword v63, v[2:3], off offset:3584
	global_load_dword v62, v[2:3], off offset:3840
	global_load_dword v61, v[4:5], off
	global_load_dword v60, v[4:5], off offset:256
	global_load_dword v59, v[4:5], off offset:512
	global_load_dword v58, v[4:5], off offset:768
	global_load_dword v57, v[4:5], off offset:1024
	global_load_dword v56, v[4:5], off offset:1280
	global_load_dword v55, v[4:5], off offset:1536
	global_load_dword v54, v[4:5], off offset:1792
	global_load_dword v53, v[4:5], off offset:2048
	global_load_dword v52, v[4:5], off offset:2304
	global_load_dword v51, v[4:5], off offset:2560
	global_load_dword v50, v[4:5], off offset:2816
	global_load_dword v49, v[4:5], off offset:3072
	global_load_dword v48, v[4:5], off offset:3328
	global_load_dword v47, v[4:5], off offset:3584
	global_load_dword v46, v[4:5], off offset:3840
	global_load_dword v45, v[6:7], off
	global_load_dword v44, v[6:7], off offset:256
	global_load_dword v43, v[6:7], off offset:512
	global_load_dword v42, v[6:7], off offset:768
	global_load_dword v41, v[6:7], off offset:1024
	global_load_dword v40, v[6:7], off offset:1280
	global_load_dword v39, v[6:7], off offset:1536
	global_load_dword v38, v[6:7], off offset:1792
	global_load_dword v37, v[6:7], off offset:2048
	global_load_dword v36, v[6:7], off offset:2304
	global_load_dword v35, v[6:7], off offset:2560
	global_load_dword v34, v[6:7], off offset:2816
	global_load_dword v33, v[6:7], off offset:3072
	global_load_dword v32, v[6:7], off offset:3328
	global_load_dword v31, v[6:7], off offset:3584
	global_load_dword v30, v[6:7], off offset:3840
	global_load_dword v29, v[8:9], off
	global_load_dword v28, v[8:9], off offset:256
	global_load_dword v27, v[8:9], off offset:512
	global_load_dword v26, v[8:9], off offset:768
	global_load_dword v25, v[8:9], off offset:1024
	global_load_dword v24, v[8:9], off offset:1280
	global_load_dword v23, v[8:9], off offset:1536
	global_load_dword v22, v[8:9], off offset:1792
	global_load_dword v21, v[8:9], off offset:2048
	global_load_dword v20, v[8:9], off offset:2304
	global_load_dword v19, v[8:9], off offset:2560
	global_load_dword v18, v[8:9], off offset:2816
	global_load_dword v17, v[8:9], off offset:3072
	global_load_dword v16, v[8:9], off offset:3328
	global_load_dword v15, v[8:9], off offset:3584
	global_load_dword v14, v[8:9], off offset:3840
	v_lshlrev_b32_e32 v11, 1, v10
	v_lshlrev_b64 v[2:3], v10, -1
	v_not_b32_e32 v12, v3
	v_not_b32_e32 v13, v2
	s_add_i32 s10, s6, 31
	s_lshr_b32 s10, s10, 10
	s_waitcnt vmcnt(0)
	s_cmp_lt_u32 s10, 4
	s_cbranch_scc0 .Lmk_hi
	s_cmp_lt_u32 s10, 2
	s_cbranch_scc0 .Lmk_23
	s_cmp_eq_u32 s10, 0
	s_cbranch_scc1 .Lmk0
	s_branch .Lmk1
.Lmk_23:
	s_cmp_eq_u32 s10, 2
	s_cbranch_scc1 .Lmk2
	s_branch .Lmk3
.Lmk_hi:
	s_cmp_lt_u32 s10, 6
	s_cbranch_scc0 .Lmk_67
	s_cmp_eq_u32 s10, 4
	s_cbranch_scc1 .Lmk4
	s_branch .Lmk5
.Lmk_67:
	s_cmp_eq_u32 s10, 6
	s_cbranch_scc1 .Lmk6
	s_branch .Lmk7
.Lmk0:
	v_cmp_gt_i32_e32 vcc, s52, v10
	v_cmp_gt_i32_e64 s[10:11], s26, v10
	s_nop 0
	v_cndmask_b32_e32 v77, 0, v77, vcc
	v_cndmask_b32_e64 v76, 0, v76, s[10:11]
	v_cmp_gt_i32_e32 vcc, s27, v10
	v_cmp_gt_i32_e64 s[10:11], s28, v10
	s_nop 0
	v_cndmask_b32_e32 v75, 0, v75, vcc
	v_cndmask_b32_e64 v74, 0, v74, s[10:11]
	v_cmp_gt_i32_e32 vcc, s29, v10
	v_cmp_gt_i32_e64 s[10:11], s30, v10
	s_nop 0
	v_cndmask_b32_e32 v73, 0, v73, vcc
	v_cndmask_b32_e64 v72, 0, v72, s[10:11]
	v_cmp_gt_i32_e32 vcc, s31, v10
	v_cmp_gt_i32_e64 s[10:11], s34, v10
	s_nop 0
	v_cndmask_b32_e32 v71, 0, v71, vcc
	v_cndmask_b32_e64 v70, 0, v70, s[10:11]
	s_branch .Lmk_done
.Lmk1:
	v_cmp_gt_i32_e32 vcc, s35, v10
	v_cmp_gt_i32_e64 s[10:11], s36, v10
	s_nop 0
	v_cndmask_b32_e32 v69, 0, v69, vcc
	v_cndmask_b32_e64 v68, 0, v68, s[10:11]
	v_cmp_gt_i32_e32 vcc, s7, v10
	v_cmp_gt_i32_e64 s[10:11], s37, v10
	s_nop 0
	v_cndmask_b32_e32 v67, 0, v67, vcc
	v_cndmask_b32_e64 v66, 0, v66, s[10:11]
	v_cmp_gt_i32_e32 vcc, s2, v10
	v_cmp_gt_i32_e64 s[10:11], s38, v10
	s_nop 0
	v_cndmask_b32_e32 v65, 0, v65, vcc
	v_cndmask_b32_e64 v64, 0, v64, s[10:11]
	v_cmp_gt_i32_e32 vcc, s39, v10
	v_cmp_gt_i32_e64 s[10:11], s40, v10
	s_nop 0
	v_cndmask_b32_e32 v63, 0, v63, vcc
	v_cndmask_b32_e64 v62, 0, v62, s[10:11]
	s_branch .Lmk_done
.Lmk2:
	v_cmp_gt_i32_e32 vcc, s41, v10
	v_cmp_gt_i32_e64 s[10:11], s42, v10
	s_nop 0
	v_cndmask_b32_e32 v61, 0, v61, vcc
	v_cndmask_b32_e64 v60, 0, v60, s[10:11]
	v_cmp_gt_i32_e32 vcc, s43, v10
	v_cmp_gt_i32_e64 s[10:11], s33, v10
	s_nop 0
	v_cndmask_b32_e32 v59, 0, v59, vcc
	v_cndmask_b32_e64 v58, 0, v58, s[10:11]
	v_cmp_gt_i32_e32 vcc, s44, v10
	v_cmp_gt_i32_e64 s[10:11], s45, v10
	s_nop 0
	v_cndmask_b32_e32 v57, 0, v57, vcc
	v_cndmask_b32_e64 v56, 0, v56, s[10:11]
	v_cmp_gt_i32_e32 vcc, s51, v10
	v_cmp_gt_i32_e64 s[10:11], s50, v10
	s_nop 0
	v_cndmask_b32_e32 v55, 0, v55, vcc
	v_cndmask_b32_e64 v54, 0, v54, s[10:11]
	s_branch .Lmk_done
.Lmk3:
	v_cmp_gt_i32_e32 vcc, s56, v10
	v_cmp_gt_i32_e64 s[10:11], s55, v10
	s_nop 0
	v_cndmask_b32_e32 v53, 0, v53, vcc
	v_cndmask_b32_e64 v52, 0, v52, s[10:11]
	v_cmp_gt_i32_e32 vcc, s58, v10
	v_cmp_gt_i32_e64 s[10:11], s57, v10
	s_nop 0
	v_cndmask_b32_e32 v51, 0, v51, vcc
	v_cndmask_b32_e64 v50, 0, v50, s[10:11]
	v_cmp_gt_i32_e32 vcc, s63, v10
	v_cmp_gt_i32_e64 s[10:11], s59, v10
	s_nop 0
	v_cndmask_b32_e32 v49, 0, v49, vcc
	v_cndmask_b32_e64 v48, 0, v48, s[10:11]
	v_cmp_gt_i32_e32 vcc, s62, v10
	v_cmp_gt_i32_e64 s[10:11], s65, v10
	s_nop 0
	v_cndmask_b32_e32 v47, 0, v47, vcc
	v_cndmask_b32_e64 v46, 0, v46, s[10:11]
	s_branch .Lmk_done
.Lmk4:
	v_cmp_gt_i32_e32 vcc, s64, v10
	v_cmp_gt_i32_e64 s[10:11], s67, v10
	s_nop 0
	v_cndmask_b32_e32 v45, 0, v45, vcc
	v_cndmask_b32_e64 v44, 0, v44, s[10:11]
	v_cmp_gt_i32_e32 vcc, s66, v10
	v_cmp_gt_i32_e64 s[10:11], s68, v10
	s_nop 0
	v_cndmask_b32_e32 v43, 0, v43, vcc
	v_cndmask_b32_e64 v42, 0, v42, s[10:11]
	v_cmp_gt_i32_e32 vcc, s69, v10
	v_cmp_gt_i32_e64 s[10:11], s70, v10
	s_nop 0
	v_cndmask_b32_e32 v41, 0, v41, vcc
	v_cndmask_b32_e64 v40, 0, v40, s[10:11]
	v_cmp_gt_i32_e32 vcc, s72, v10
	v_cmp_gt_i32_e64 s[10:11], s71, v10
	s_nop 0
	v_cndmask_b32_e32 v39, 0, v39, vcc
	v_cndmask_b32_e64 v38, 0, v38, s[10:11]
	s_branch .Lmk_done
.Lmk5:
	v_cmp_gt_i32_e32 vcc, s73, v10
	v_cmp_gt_i32_e64 s[10:11], s74, v10
	s_nop 0
	v_cndmask_b32_e32 v37, 0, v37, vcc
	v_cndmask_b32_e64 v36, 0, v36, s[10:11]
	v_cmp_gt_i32_e32 vcc, s75, v10
	v_cmp_gt_i32_e64 s[10:11], s76, v10
	s_nop 0
	v_cndmask_b32_e32 v35, 0, v35, vcc
	v_cndmask_b32_e64 v34, 0, v34, s[10:11]
	v_cmp_gt_i32_e32 vcc, s77, v10
	v_cmp_gt_i32_e64 s[10:11], s78, v10
	s_nop 0
	v_cndmask_b32_e32 v33, 0, v33, vcc
	v_cndmask_b32_e64 v32, 0, v32, s[10:11]
	v_cmp_gt_i32_e32 vcc, s79, v10
	v_cmp_gt_i32_e64 s[10:11], s96, v10
	s_nop 0
	v_cndmask_b32_e32 v31, 0, v31, vcc
	v_cndmask_b32_e64 v30, 0, v30, s[10:11]
	s_branch .Lmk_done
.Lmk6:
	v_cmp_gt_i32_e32 vcc, s82, v10
	v_cmp_gt_i32_e64 s[10:11], s83, v10
	s_nop 0
	v_cndmask_b32_e32 v29, 0, v29, vcc
	v_cndmask_b32_e64 v28, 0, v28, s[10:11]
	v_cmp_gt_i32_e32 vcc, s84, v10
	v_cmp_gt_i32_e64 s[10:11], s85, v10
	s_nop 0
	v_cndmask_b32_e32 v27, 0, v27, vcc
	v_cndmask_b32_e64 v26, 0, v26, s[10:11]
	v_cmp_gt_i32_e32 vcc, s86, v10
	v_cmp_gt_i32_e64 s[10:11], s87, v10
	s_nop 0
	v_cndmask_b32_e32 v25, 0, v25, vcc
	v_cndmask_b32_e64 v24, 0, v24, s[10:11]
	v_cmp_gt_i32_e32 vcc, s88, v10
	v_cmp_gt_i32_e64 s[10:11], s89, v10
	s_nop 0
	v_cndmask_b32_e32 v23, 0, v23, vcc
	v_cndmask_b32_e64 v22, 0, v22, s[10:11]
	s_branch .Lmk_done
.Lmk7:
	v_cmp_gt_i32_e32 vcc, s90, v10
	v_cmp_gt_i32_e64 s[10:11], s91, v10
	s_nop 0
	v_cndmask_b32_e32 v21, 0, v21, vcc
	v_cndmask_b32_e64 v20, 0, v20, s[10:11]
	v_cmp_gt_i32_e32 vcc, s92, v10
	v_cmp_gt_i32_e64 s[10:11], s94, v10
	s_nop 0
	v_cndmask_b32_e32 v19, 0, v19, vcc
	v_cndmask_b32_e64 v18, 0, v18, s[10:11]
	v_readlane_b32 s9, v255, 16
	v_readlane_b32 s8, v255, 17
	s_nop 1
	v_cmp_gt_i32_e32 vcc, s9, v10
	v_cmp_gt_i32_e64 s[10:11], s8, v10
	s_nop 0
	v_cndmask_b32_e32 v17, 0, v17, vcc
	v_cndmask_b32_e64 v16, 0, v16, s[10:11]
	v_readlane_b32 s9, v255, 18
	v_readlane_b32 s8, v255, 19
	s_nop 1
	v_cmp_gt_i32_e32 vcc, s9, v10
	v_cmp_gt_i32_e64 s[10:11], s8, v10
	s_nop 0
	v_cndmask_b32_e32 v15, 0, v15, vcc
	v_cndmask_b32_e64 v14, 0, v14, s[10:11]
.Lmk_done:
	v_readlane_b32 s8, v255, 19
	s_cmpk_lt_i32 s97, 0x100
	s_cbranch_scc1 .LBB0_759
	s_lshl_b32 s0, s0, 11
	s_add_i32 s0, s0, 0
	v_lshl_add_u32 v6, v10, 5, s0
	ds_read_b128 v[2:5], v6
	ds_read_b128 v[6:9], v6 offset:16
	s_mov_b32 s83, s78
	s_mov_b32 s77, s76
	s_mov_b32 s75, s74
	s_waitcnt lgkmcnt(1)
	v_add_u32_e32 v78, v2, v3
	v_add3_u32 v78, v78, v5, v4
	s_waitcnt lgkmcnt(0)
	v_add3_u32 v78, v78, v9, v8
	s_mov_b32 s73, s72
	s_mov_b32 s72, s70
	s_mov_b32 s76, s65
	s_mov_b32 s74, s63
	s_mov_b32 s69, s62
	s_mov_b32 s68, s58
	s_mov_b32 s66, s56
	s_mov_b32 s65, s55
	s_mov_b32 s64, s6
	s_mov_b32 s6, s51
	s_mov_b32 s58, s50
	s_mov_b64 s[62:63], s[48:49]
	s_mov_b32 s56, s43
	s_mov_b32 s49, s42
	s_mov_b32 s48, s41
	s_mov_b32 s91, s40
	s_mov_b32 s90, s39
	s_mov_b32 s89, s38
	s_mov_b32 s88, s2
	s_mov_b32 s2, s37
	s_mov_b32 s84, s7
	s_mov_b32 s7, s36
	s_mov_b32 s85, s35
	s_mov_b32 s44, s34
	s_mov_b32 s51, s31
	s_mov_b32 s50, s30
	s_mov_b32 s92, s29
	s_mov_b32 s71, s28
	s_mov_b32 s70, s27
	s_mov_b32 s81, s26
	s_mov_b32 s82, s25
	s_mov_b32 s55, s22
	v_add3_u32 v78, v78, v7, v6
	s_mov_b32 s9, 63
	s_nop 0
	v_readlane_b32 s25, v78, 63
	v_readlane_b32 s26, v78, 62
	v_readlane_b32 s27, v78, 61
	v_readlane_b32 s28, v78, 60
	v_readlane_b32 s29, v78, 59
	v_readlane_b32 s30, v78, 58
	v_readlane_b32 s31, v78, 57
	v_readlane_b32 s34, v78, 56
	v_readlane_b32 s35, v78, 55
	v_readlane_b32 s36, v78, 54
	v_readlane_b32 s37, v78, 53
	v_readlane_b32 s38, v78, 52
	v_readlane_b32 s39, v78, 51
	v_readlane_b32 s40, v78, 50
	v_readlane_b32 s41, v78, 49
	v_readlane_b32 s42, v78, 48
	s_mov_b32 s8, s1
	s_add_i32 s1, s8, s25
	s_cmpk_gt_u32 s1, 0xff
	s_cbranch_scc1 .Lthr_f63
	s_mov_b32 s8, s1
	s_add_i32 s1, s8, s26
	s_cmpk_gt_u32 s1, 0xff
	s_cbranch_scc1 .Lthr_f62
	s_mov_b32 s8, s1
	s_add_i32 s1, s8, s27
	s_cmpk_gt_u32 s1, 0xff
	s_cbranch_scc1 .Lthr_f61
	s_mov_b32 s8, s1
	s_add_i32 s1, s8, s28
	s_cmpk_gt_u32 s1, 0xff
	s_cbranch_scc1 .Lthr_f60
	s_mov_b32 s8, s1
	s_add_i32 s1, s8, s29
	s_cmpk_gt_u32 s1, 0xff
	s_cbranch_scc1 .Lthr_f59
	s_mov_b32 s8, s1
	s_add_i32 s1, s8, s30
	s_cmpk_gt_u32 s1, 0xff
	s_cbranch_scc1 .Lthr_f58
	s_mov_b32 s8, s1
	s_add_i32 s1, s8, s31
	s_cmpk_gt_u32 s1, 0xff
	s_cbranch_scc1 .Lthr_f57
	s_mov_b32 s8, s1
	s_add_i32 s1, s8, s34
	s_cmpk_gt_u32 s1, 0xff
	s_cbranch_scc1 .Lthr_f56
	s_mov_b32 s8, s1
	s_add_i32 s1, s8, s35
	s_cmpk_gt_u32 s1, 0xff
	s_cbranch_scc1 .Lthr_f55
	s_mov_b32 s8, s1
	s_add_i32 s1, s8, s36
	s_cmpk_gt_u32 s1, 0xff
	s_cbranch_scc1 .Lthr_f54
	s_mov_b32 s8, s1
	s_add_i32 s1, s8, s37
	s_cmpk_gt_u32 s1, 0xff
	s_cbranch_scc1 .Lthr_f53
	s_mov_b32 s8, s1
	s_add_i32 s1, s8, s38
	s_cmpk_gt_u32 s1, 0xff
	s_cbranch_scc1 .Lthr_f52
	s_mov_b32 s8, s1
	s_add_i32 s1, s8, s39
	s_cmpk_gt_u32 s1, 0xff
	s_cbranch_scc1 .Lthr_f51
	s_mov_b32 s8, s1
	s_add_i32 s1, s8, s40
	s_cmpk_gt_u32 s1, 0xff
	s_cbranch_scc1 .Lthr_f50
	s_mov_b32 s8, s1
	s_add_i32 s1, s8, s41
	s_cmpk_gt_u32 s1, 0xff
	s_cbranch_scc1 .Lthr_f49
	s_mov_b32 s8, s1
	s_add_i32 s1, s8, s42
	s_cmpk_gt_u32 s1, 0xff
	s_cbranch_scc1 .Lthr_f48
	s_mov_b32 s8, s1
	s_mov_b32 s9, 47
	s_branch .LBB0_723
